# P0/P2/P6 RMS norms: 1/sqrt via one f32 v_rsq_f32 instead of the expanded IEEE sqrt+divide chain (as in the NA staging)
# speedup vs baseline: 1.0044x; 1.0044x over previous
.LBB0_96:
	s_mov_b64 s[4:5], s[64:65]
	v_cmp_lt_i32_e32 vcc, v10, v9
	s_load_dwordx2 s[2:3], s[4:5], 0x0
	s_mov_b64 s[14:15], s[64:65]
	v_cndmask_b32_e32 v0, v8, v10, vcc
	v_cmp_lt_i32_e32 vcc, v11, v9
	s_load_dwordx2 s[4:5], s[14:15], 0x8
	s_waitcnt vmcnt(4) lgkmcnt(0)
	v_lshl_add_u64 v[30:31], s[2:3], 0, v[6:7]
	v_cndmask_b32_e32 v1, v8, v11, vcc
	v_cmp_lt_i32_e32 vcc, v12, v9
	v_lshlrev_b32_e32 v59, 2, v0
	v_lshlrev_b32_e32 v60, 2, v1
	v_cndmask_b32_e32 v2, v8, v12, vcc
	v_cmp_lt_i32_e32 vcc, v13, v9
	v_lshlrev_b32_e32 v61, 2, v2
	v_lshl_add_u64 v[56:57], v[32:33], 4, s[4:5]
	v_cndmask_b32_e32 v3, v8, v13, vcc
	v_cmp_lt_i32_e32 vcc, v14, v9
	v_lshlrev_b32_e32 v62, 2, v3
	v_mov_b32_e32 v58, 0
	v_cndmask_b32_e32 v18, v8, v14, vcc
	v_cmp_lt_i32_e32 vcc, v15, v9
	v_lshlrev_b32_e32 v63, 2, v18
	s_add_i32 s6, s6, s8
	v_cndmask_b32_e32 v19, v8, v15, vcc
	v_lshlrev_b32_e32 v64, 2, v19
	global_load_dwordx4 v[18:21], v[30:31], off offset:-4096
	global_load_dwordx4 v[22:25], v[30:31], off offset:-3072
	global_load_dwordx4 v[26:29], v[30:31], off offset:-2048
	global_load_dwordx4 v[34:37], v[30:31], off offset:-1024
	v_add_co_u32_e32 v54, vcc, 0xfffff000, v30
	s_cmpk_gt_i32 s6, 0x7fff
	s_nop 0
	v_addc_co_u32_e32 v55, vcc, -1, v31, vcc
	global_load_dwordx4 v[38:41], v[54:55], off offset:-3072
	global_load_dwordx4 v[42:45], v[54:55], off offset:-2048
	global_load_dwordx4 v[46:49], v[54:55], off offset:-1024
	global_load_dwordx4 v[0:3], v[30:31], off
	global_load_dwordx4 v[50:53], v[56:57], off
	v_lshl_add_u64 v[6:7], v[6:7], 0, s[12:13]
	s_waitcnt vmcnt(8)
	v_mul_f32_e32 v30, v19, v19
	v_mul_f32_e32 v31, v21, v21
	s_waitcnt vmcnt(7)
	v_mul_f32_e32 v54, v23, v23
	v_mul_f32_e32 v55, v25, v25
	s_waitcnt vmcnt(6)
	v_mul_f32_e32 v65, v27, v27
	v_mul_f32_e32 v66, v29, v29
	s_waitcnt vmcnt(5)
	v_mul_f32_e32 v67, v35, v35
	v_mul_f32_e32 v68, v37, v37
	v_fmac_f32_e32 v30, v18, v18
	v_fmac_f32_e32 v31, v20, v20
	v_fmac_f32_e32 v54, v22, v22
	v_fmac_f32_e32 v55, v24, v24
	v_fmac_f32_e32 v65, v26, v26
	v_fmac_f32_e32 v66, v28, v28
	s_waitcnt vmcnt(4)
	v_mul_f32_e32 v69, v39, v39
	v_mul_f32_e32 v70, v41, v41
	s_waitcnt vmcnt(3)
	v_mul_f32_e32 v71, v43, v43
	v_mul_f32_e32 v72, v45, v45
	v_fmac_f32_e32 v67, v34, v34
	v_fmac_f32_e32 v68, v36, v36
	s_waitcnt vmcnt(2)
	v_mul_f32_e32 v73, v47, v47
	v_mul_f32_e32 v74, v49, v49
	v_add_f32_e32 v30, v30, v31
	v_add_f32_e32 v31, v54, v55
	v_add_f32_e32 v54, v65, v66
	s_waitcnt vmcnt(1)
	v_mul_f32_e32 v65, v1, v1
	v_mul_f32_e32 v66, v3, v3
	v_fmac_f32_e32 v69, v38, v38
	v_fmac_f32_e32 v70, v40, v40
	v_fmac_f32_e32 v71, v42, v42
	v_fmac_f32_e32 v72, v44, v44
	v_add_f32_e32 v55, v67, v68
	v_fmac_f32_e32 v73, v46, v46
	v_fmac_f32_e32 v74, v48, v48
	v_fmac_f32_e32 v65, v0, v0
	v_fmac_f32_e32 v66, v2, v2
	v_add_f32_e32 v67, v69, v70
	v_add_f32_e32 v68, v71, v72
	v_add_f32_e32 v69, v73, v74
	v_add_f32_e32 v65, v65, v66
	v_add_f32_e32 v66, v67, v68
	v_add_f32_e32 v66, v66, v69
	v_add_f32_e32 v30, v66, v30
	v_add_f32_e32 v30, v30, v31
	v_add_f32_e32 v30, v30, v54
	v_add_f32_e32 v30, v30, v55
	v_add_f32_e32 v30, v30, v65
	ds_bpermute_b32 v31, v59, v30
	s_waitcnt lgkmcnt(0)
	v_add_f32_e32 v30, v30, v31
	ds_bpermute_b32 v31, v60, v30
	s_waitcnt lgkmcnt(0)
	v_add_f32_e32 v30, v30, v31
	ds_bpermute_b32 v31, v61, v30
	s_waitcnt lgkmcnt(0)
	v_add_f32_e32 v30, v30, v31
	ds_bpermute_b32 v31, v62, v30
	s_waitcnt lgkmcnt(0)
	v_add_f32_e32 v30, v30, v31
	ds_bpermute_b32 v31, v63, v30
	s_waitcnt lgkmcnt(0)
	v_add_f32_e32 v30, v30, v31
	ds_bpermute_b32 v31, v64, v30
	s_waitcnt lgkmcnt(0)
	v_add_f32_e32 v30, v30, v31
	v_fmamk_f32 v30, v30, 0x3a000000, v16
	v_rsq_f32_e32 v54, v30
	s_nop 0
	v_mul_f32_e32 v30, v38, v54
	v_mul_f32_e32 v31, v39, v54
	s_waitcnt vmcnt(0)
	v_mul_f32_e32 v30, v50, v30
	v_mul_f32_e32 v31, v51, v31
	v_cvt_pk_fp8_f32 v58, v30, v31
	v_mul_f32_e32 v38, v40, v54
	v_mul_f32_e32 v39, v41, v54
	v_mul_f32_e32 v38, v52, v38
	v_mul_f32_e32 v39, v53, v39
	v_cvt_pk_fp8_f32 v58, v38, v39 op_sel:[0,0,1]
	v_mul_f32_e32 v31, v42, v54
	v_mul_f32_e32 v42, v43, v54
	v_mov_b32_e32 v30, 0
	global_store_dword v[4:5], v58, off
	global_load_dwordx4 v[38:41], v[56:57], off offset:1024
	v_mul_f32_e32 v43, v44, v54
	v_mul_f32_e32 v44, v45, v54
	v_mul_f32_e32 v18, v18, v54
	v_mul_f32_e32 v19, v19, v54
	v_mul_f32_e32 v20, v20, v54
	v_mul_f32_e32 v21, v21, v54
	v_mul_f32_e32 v22, v22, v54
	v_mul_f32_e32 v23, v23, v54
	v_mul_f32_e32 v24, v24, v54
	v_mul_f32_e32 v25, v25, v54
	v_mul_f32_e32 v0, v0, v54
	v_mul_f32_e32 v1, v1, v54
	v_mul_f32_e32 v2, v2, v54
	v_mul_f32_e32 v3, v3, v54
	s_waitcnt vmcnt(0)
	v_mul_f32_e32 v31, v38, v31
	v_mul_f32_e32 v38, v39, v42
	v_cvt_pk_fp8_f32 v30, v31, v38
	v_mul_f32_e32 v39, v40, v43
	v_mul_f32_e32 v40, v41, v44
	v_mul_f32_e32 v31, v46, v54
	v_cvt_pk_fp8_f32 v30, v39, v40 op_sel:[0,0,1]
	v_mul_f32_e32 v42, v47, v54
	v_mul_f32_e32 v43, v48, v54
	v_mul_f32_e32 v44, v49, v54
	global_store_dword v[4:5], v30, off offset:256
	global_load_dwordx4 v[38:41], v[56:57], off offset:2048
	v_mov_b32_e32 v30, 0
	s_waitcnt vmcnt(0)
	v_mul_f32_e32 v31, v31, v38
	v_mul_f32_e32 v38, v42, v39
	v_cvt_pk_fp8_f32 v30, v31, v38
	v_mul_f32_e32 v39, v43, v40
	v_mul_f32_e32 v40, v44, v41
	v_mov_b32_e32 v42, 0
	v_cvt_pk_fp8_f32 v30, v39, v40 op_sel:[0,0,1]
	global_store_dword v[4:5], v30, off offset:512
	global_load_dwordx4 v[38:41], v[56:57], off offset:3072
	v_add_co_u32_e32 v30, vcc, s1, v56
	s_waitcnt vmcnt(0)
	v_mul_f32_e32 v18, v18, v38
	v_mul_f32_e32 v19, v19, v39
	v_cvt_pk_fp8_f32 v42, v18, v19
	v_mul_f32_e32 v20, v20, v40
	v_mul_f32_e32 v21, v21, v41
	v_addc_co_u32_e32 v31, vcc, 0, v57, vcc
	v_cvt_pk_fp8_f32 v42, v20, v21 op_sel:[0,0,1]
	v_mov_b32_e32 v38, 0
	global_store_dword v[4:5], v42, off offset:768
	global_load_dwordx4 v[18:21], v[30:31], off
	s_waitcnt vmcnt(0)
	v_mul_f32_e32 v18, v22, v18
	v_mul_f32_e32 v19, v23, v19
	v_cvt_pk_fp8_f32 v38, v18, v19
	v_mul_f32_e32 v20, v24, v20
	v_mul_f32_e32 v21, v25, v21
	v_mul_f32_e32 v23, v26, v54
	v_cvt_pk_fp8_f32 v38, v20, v21 op_sel:[0,0,1]
	v_mul_f32_e32 v24, v27, v54
	v_mov_b32_e32 v22, 0
	v_mul_f32_e32 v25, v28, v54
	global_store_dword v[4:5], v38, off offset:1024
	global_load_dwordx4 v[18:21], v[30:31], off offset:1024
	v_mul_f32_e32 v26, v29, v54
	s_waitcnt vmcnt(0)
	v_mul_f32_e32 v18, v23, v18
	v_mul_f32_e32 v19, v24, v19
	v_cvt_pk_fp8_f32 v22, v18, v19
	v_mul_f32_e32 v20, v25, v20
	v_mul_f32_e32 v21, v26, v21
	v_mul_f32_e32 v23, v34, v54
	v_cvt_pk_fp8_f32 v22, v20, v21 op_sel:[0,0,1]
	v_mul_f32_e32 v24, v35, v54
	v_mul_f32_e32 v25, v36, v54
	v_mul_f32_e32 v26, v37, v54
	global_store_dword v[4:5], v22, off offset:1280
	global_load_dwordx4 v[18:21], v[30:31], off offset:2048
	v_mov_b32_e32 v22, 0
	s_waitcnt vmcnt(0)
	v_mul_f32_e32 v18, v23, v18
	v_mul_f32_e32 v19, v24, v19
	v_cvt_pk_fp8_f32 v22, v18, v19
	v_mul_f32_e32 v20, v25, v20
	v_mul_f32_e32 v18, v26, v21
	v_cvt_pk_fp8_f32 v22, v20, v18 op_sel:[0,0,1]
	global_store_dword v[4:5], v22, off offset:1536
	global_load_dwordx4 v[18:21], v[30:31], off offset:3072
	v_mov_b32_e32 v22, 0
	s_waitcnt vmcnt(0)
	v_mul_f32_e32 v0, v0, v18
	v_mul_f32_e32 v1, v1, v19
	v_cvt_pk_fp8_f32 v22, v0, v1
	v_mul_f32_e32 v0, v2, v20
	v_mul_f32_e32 v1, v3, v21
	v_cvt_pk_fp8_f32 v22, v0, v1 op_sel:[0,0,1]
	global_store_dword v[4:5], v22, off offset:1792
	v_lshl_add_u64 v[4:5], v[4:5], 0, s[10:11]
	s_cbranch_scc0 .LBB0_96

.LBB0_306:
	s_waitcnt lgkmcnt(0)
	global_load_dwordx4 v[0:3], v42, s[10:11] offset:16
	global_load_dwordx4 v[4:7], v42, s[10:11]
	v_add_u32_e32 v32, s26, v13
	s_lshr_b32 s98, s20, 26
	s_lshr_b32 s99, s26, 4
	s_and_b32 s98, s98, s99
	s_bfe_i32 s98, s98, 0x10000
	v_mbcnt_lo_u32_b32 v201, -1, 0
	v_mbcnt_hi_u32_b32 v201, -1, v201
	v_and_b32_e32 v201, 2, v201
	v_lshlrev_b32_e32 v201, 2, v201
	v_and_b32_e32 v202, s98, v201
	v_mov_b32_e32 v203, 0
	v_cvt_f32_fp8_e32 v49, v8
	v_cvt_f32_fp8_sdwa v62, v8 src0_sel:BYTE_1
	v_cvt_f32_fp8_sdwa v63, v8 src0_sel:BYTE_2
	v_cvt_f32_fp8_sdwa v64, v8 src0_sel:BYTE_3
	v_cvt_f32_fp8_e32 v65, v9
	v_cvt_f32_fp8_sdwa v66, v9 src0_sel:BYTE_1
	v_cvt_f32_fp8_sdwa v67, v9 src0_sel:BYTE_2
	v_cvt_f32_fp8_sdwa v68, v9 src0_sel:BYTE_3
	v_and_b32_e32 v8, 63, v32
	v_bfe_u32 v9, v32, 6, 8
	v_and_b32_e32 v11, 64, v41
	v_cndmask_b32_e64 v8, v8, v9, s[4:5]
	v_xor_b32_e32 v10, 1, v41
	v_add_u32_e32 v33, 64, v11
	v_lshlrev_b32_e32 v8, 7, v8
	v_mov_b32_e32 v9, v15
	v_cmp_lt_i32_e32 vcc, v10, v33
	v_lshl_add_u64 v[30:31], v[20:21], 0, v[8:9]
	v_lshl_add_u64 v[46:47], v[30:31], 0, v[14:15]
	v_cndmask_b32_e32 v10, v41, v10, vcc
	v_lshlrev_b32_e32 v45, 2, v10
	global_load_dwordx4 v[8:11], v[46:47], off offset:16
	global_load_dwordx4 v[50:53], v[46:47], off
	global_load_dwordx4 v[54:57], v[30:31], off offset:16
	global_load_dwordx4 v[58:61], v[30:31], off
	v_mul_f32_e32 v69, v62, v62
	v_fmac_f32_e32 v69, v49, v49
	v_fmac_f32_e32 v69, v63, v63
	v_fmac_f32_e32 v69, v64, v64
	v_fmac_f32_e32 v69, v65, v65
	v_fmac_f32_e32 v69, v66, v66
	v_fmac_f32_e32 v69, v67, v67
	v_fmac_f32_e32 v69, v68, v68
	ds_bpermute_b32 v70, v45, v69
	v_xor_b32_e32 v48, 2, v41
	v_cmp_lt_i32_e32 vcc, v48, v33
	v_xor_b32_e32 v46, 4, v41
	s_nop 0
	v_cndmask_b32_e32 v30, v41, v48, vcc
	v_lshlrev_b32_e32 v47, 2, v30
	s_waitcnt lgkmcnt(0)
	v_add_f32_e32 v30, v69, v70
	ds_bpermute_b32 v31, v47, v30
	v_cmp_lt_i32_e32 vcc, v46, v33
	v_xor_b32_e32 v48, 8, v41
	s_waitcnt lgkmcnt(0)
	v_add_f32_e32 v30, v30, v31
	v_cndmask_b32_e32 v46, v41, v46, vcc
	v_lshlrev_b32_e32 v46, 2, v46
	ds_bpermute_b32 v31, v46, v30
	v_cmp_lt_i32_e32 vcc, v48, v33
	s_waitcnt lgkmcnt(0)
	v_add_f32_e32 v30, v30, v31
	v_cndmask_b32_e32 v33, v41, v48, vcc
	v_lshlrev_b32_e32 v48, 2, v33
	ds_bpermute_b32 v31, v48, v30
	s_waitcnt lgkmcnt(0)
	v_add_f32_e32 v30, v30, v31
	v_fmamk_f32 v30, v30, 0x3c000000, v38
	v_rsq_f32_e32 v33, v30
	s_nop 0
	v_lshl_add_u64 v[30:31], v[22:23], 0, s[20:21]
	v_mul_f32_e32 v49, v49, v33
	s_waitcnt vmcnt(4)
	v_mul_f32_e32 v49, v4, v49
	ds_bpermute_b32 v69, v46, v49
	v_mul_f32_e32 v63, v63, v33
	v_mul_f32_e32 v63, v6, v63
	v_mul_f32_e32 v65, v65, v33
	v_mul_f32_e32 v65, v0, v65
	s_waitcnt vmcnt(2) lgkmcnt(0)
	v_mul_f32_e32 v50, v50, v69
	v_cndmask_b32_e64 v50, v50, -v50, s[6:7]
	s_waitcnt vmcnt(0)
	v_fmac_f32_e32 v50, v58, v49
	ds_bpermute_b32 v49, v46, v63
	v_mul_f32_e32 v64, v64, v33
	v_mul_f32_e32 v64, v7, v64
	ds_bpermute_b32 v58, v46, v64
	v_mul_f32_e32 v62, v62, v33
	s_waitcnt lgkmcnt(1)
	v_mul_f32_e32 v49, v52, v49
	ds_bpermute_b32 v52, v46, v65
	v_mul_f32_e32 v62, v5, v62
	v_mul_f32_e32 v67, v67, v33
	v_mul_f32_e32 v66, v66, v33
	v_mul_f32_e32 v67, v2, v67
	v_mul_f32_e32 v33, v68, v33
	ds_bpermute_b32 v68, v46, v62
	v_mul_f32_e32 v66, v1, v66
	s_waitcnt lgkmcnt(1)
	v_mul_f32_e32 v8, v8, v52
	ds_bpermute_b32 v52, v46, v67
	v_mul_f32_e32 v53, v53, v58
	ds_bpermute_b32 v58, v46, v66
	v_mul_f32_e32 v33, v3, v33
	s_waitcnt lgkmcnt(2)
	v_mul_f32_e32 v51, v51, v68
	v_cndmask_b32_e64 v51, v51, -v51, s[6:7]
	s_waitcnt lgkmcnt(1)
	v_mul_f32_e32 v10, v10, v52
	ds_bpermute_b32 v52, v46, v33
	v_fmac_f32_e32 v51, v59, v62
	s_waitcnt lgkmcnt(1)
	v_mul_f32_e32 v9, v9, v58
	v_cndmask_b32_e64 v8, v8, -v8, s[6:7]
	v_cndmask_b32_e64 v9, v9, -v9, s[6:7]
	v_mul_f32_e32 v50, s25, v50
	v_mul_f32_e32 v51, s25, v51
	v_fmac_f32_e32 v8, v54, v65
	v_fmac_f32_e32 v9, v55, v66
	v_med3_f32 v50, v50, s2, v40
	v_med3_f32 v51, v51, s2, v40
	v_mov_b32_e32 v54, v15
	v_cndmask_b32_e64 v49, v49, -v49, s[6:7]
	v_cndmask_b32_e64 v53, v53, -v53, s[6:7]
	v_cvt_pk_fp8_f32 v54, v50, v51
	v_mul_f32_e32 v8, s25, v8
	v_mul_f32_e32 v9, s25, v9
	v_fmac_f32_e32 v49, v60, v63
	v_fmac_f32_e32 v53, v61, v64
	s_waitcnt lgkmcnt(0)
	v_mul_f32_e32 v11, v11, v52
	v_med3_f32 v8, v8, s2, v40
	v_med3_f32 v9, v9, s2, v40
	v_mov_b32_e32 v51, v15
	v_cndmask_b32_e64 v10, v10, -v10, s[6:7]
	v_mul_f32_e32 v49, s25, v49
	v_mul_f32_e32 v50, s25, v53
	v_cndmask_b32_e64 v11, v11, -v11, s[6:7]
	v_cvt_pk_fp8_f32 v51, v8, v9
	v_fmac_f32_e32 v10, v56, v67
	v_med3_f32 v49, v49, s2, v40
	v_med3_f32 v50, v50, s2, v40
	v_fmac_f32_e32 v11, v57, v33
	v_cvt_pk_fp8_f32 v54, v49, v50 op_sel:[0,0,1]
	v_mul_f32_e32 v8, s25, v10
	v_mul_f32_e32 v9, s25, v11
	v_med3_f32 v8, v8, s2, v40
	v_med3_f32 v9, v9, s2, v40
	v_cvt_pk_fp8_f32 v51, v8, v9 op_sel:[0,0,1]
	v_lshrrev_b32_e32 v49, 2, v54
	v_and_b32_e32 v33, 0x1f1f1f1f, v54
	v_and_b32_e32 v49, 0x20202020, v49
	v_or_b32_e32 v50, v49, v33
	v_and_b32_e32 v9, 0x1f1f1f1f, v51
	v_lshrrev_b32_e32 v10, 2, v51
	v_bitop3_b32 v33, v49, 63, v33 bitop3:0xc8
	v_lshrrev_b32_e32 v49, 2, v50
	v_and_or_b32 v9, v10, s3, v9
	v_and_or_b32 v33, v49, s13, v33
	v_lshrrev_b32_e32 v49, 4, v50
	v_lshrrev_b32_e32 v8, 6, v50
	v_lshrrev_b32_e32 v10, 2, v9
	v_and_b32_e32 v49, 0x3f000, v49
	v_and_b32_e32 v8, 0xfc0000, v8
	v_and_b32_e32 v10, 0xfc0, v10
	v_or3_b32 v8, v33, v49, v8
	v_or_b32_e32 v11, v10, v9
	v_lshrrev_b32_e32 v33, 4, v9
	v_lshrrev_b32_e32 v9, 6, v9
	v_and_b32_e32 v33, 0x3f000, v33
	v_and_b32_e32 v9, 0xfc0000, v9
	v_or3_b32 v9, v33, v9, v10
	v_lshl_or_b32 v8, v11, 24, v8
	v_lshrrev_b32_e32 v9, 8, v9
	v_mov_b32_e32 v10, v15
	v_mov_b32_e32 v11, v15
	s_nop 0
	v_mov_b32_dpp v10, v8 quad_perm:[1,0,3,2] row_mask:0xf bank_mask:0xf
	v_mov_b32_dpp v11, v9 quad_perm:[1,0,3,2] row_mask:0xf bank_mask:0xf
	s_and_saveexec_b64 s[10:11], s[8:9]
	s_cbranch_execz .LBB0_308
	v_ashrrev_i32_e32 v33, 31, v32
	v_lshlrev_b64 v[50:51], 7, v[32:33]
	v_lshl_add_u64 v[50:51], v[30:31], 0, v[50:51]
	v_lshl_or_b32 v9, v10, 16, v9
	v_perm_b32 v10, v10, v11, s15
	global_store_dword v[50:51], v8, off
	v_lshl_add_u64 v[204:205], v[50:51], 0, v[202:203]
	global_store_dword v[204:205], v9, off offset:4
	global_store_dword v[204:205], v10, off offset:8
.LBB0_308:
	s_or_b64 exec, exec, s[10:11]
	v_cvt_f32_fp8_sdwa v33, v36 src0_sel:BYTE_1
	v_cvt_f32_fp8_e32 v11, v36
	v_cvt_f32_fp8_sdwa v49, v36 src0_sel:BYTE_2
	v_cvt_f32_fp8_sdwa v66, v36 src0_sel:BYTE_3
	v_cvt_f32_fp8_e32 v67, v37
	v_mul_f32_e32 v58, v33, v33
	v_cvt_f32_fp8_sdwa v68, v37 src0_sel:BYTE_1
	v_fmac_f32_e32 v58, v11, v11
	v_cvt_f32_fp8_sdwa v69, v37 src0_sel:BYTE_2
	v_fmac_f32_e32 v58, v49, v49
	v_add_u32_e32 v10, 4, v32
	v_cvt_f32_fp8_sdwa v70, v37 src0_sel:BYTE_3
	v_fmac_f32_e32 v58, v66, v66
	v_and_b32_e32 v8, 63, v10
	v_bfe_u32 v9, v10, 6, 8
	v_fmac_f32_e32 v58, v67, v67
	v_cndmask_b32_e64 v8, v8, v9, s[4:5]
	v_fmac_f32_e32 v58, v68, v68
	v_lshlrev_b32_e32 v8, 7, v8
	v_mov_b32_e32 v9, v15
	v_fmac_f32_e32 v58, v69, v69
	v_lshl_add_u64 v[8:9], v[20:21], 0, v[8:9]
	v_fmac_f32_e32 v58, v70, v70
	v_lshl_add_u64 v[36:37], v[8:9], 0, v[14:15]
	global_load_dwordx4 v[50:53], v[36:37], off
	global_load_dwordx4 v[54:57], v[8:9], off
	ds_bpermute_b32 v59, v45, v58
	s_waitcnt lgkmcnt(0)
	v_add_f32_e32 v58, v58, v59
	ds_bpermute_b32 v59, v47, v58
	s_waitcnt lgkmcnt(0)
	v_add_f32_e32 v71, v58, v59
	global_load_dwordx4 v[58:61], v[36:37], off offset:16
	global_load_dwordx4 v[62:65], v[8:9], off offset:16
	ds_bpermute_b32 v72, v46, v71
	s_waitcnt lgkmcnt(0)
	v_add_f32_e32 v8, v71, v72
	ds_bpermute_b32 v9, v48, v8
	s_waitcnt lgkmcnt(0)
	v_add_f32_e32 v8, v8, v9
	v_fmamk_f32 v8, v8, 0x3c000000, v38
	v_rsq_f32_e32 v8, v8
	s_nop 0
	v_mul_f32_e32 v9, v11, v8
	v_mul_f32_e32 v9, v4, v9
	v_mul_f32_e32 v11, v67, v8
	v_mul_f32_e32 v33, v33, v8
	ds_bpermute_b32 v67, v46, v9
	v_mul_f32_e32 v37, v49, v8
	v_mul_f32_e32 v33, v5, v33
	v_mul_f32_e32 v36, v68, v8
	v_mul_f32_e32 v37, v6, v37
	ds_bpermute_b32 v68, v46, v33
	v_mul_f32_e32 v49, v69, v8
	ds_bpermute_b32 v69, v46, v37
	s_waitcnt vmcnt(3) lgkmcnt(2)
	v_mul_f32_e32 v50, v50, v67
	v_cndmask_b32_e64 v50, v50, -v50, s[6:7]
	v_mul_f32_e32 v66, v66, v8
	s_waitcnt vmcnt(2)
	v_fmac_f32_e32 v50, v54, v9
	s_waitcnt lgkmcnt(1)
	v_mul_f32_e32 v9, v51, v68
	v_mul_f32_e32 v66, v7, v66
	v_cndmask_b32_e64 v9, v9, -v9, s[6:7]
	s_waitcnt lgkmcnt(0)
	v_mul_f32_e32 v51, v52, v69
	v_mul_f32_e32 v11, v0, v11
	v_fmac_f32_e32 v9, v55, v33
	ds_bpermute_b32 v33, v46, v66
	v_cndmask_b32_e64 v51, v51, -v51, s[6:7]
	v_fmac_f32_e32 v51, v56, v37
	ds_bpermute_b32 v37, v46, v11
	v_mul_f32_e32 v36, v1, v36
	ds_bpermute_b32 v52, v46, v36
	v_mul_f32_e32 v49, v2, v49
	s_waitcnt lgkmcnt(2)
	v_mul_f32_e32 v33, v53, v33
	ds_bpermute_b32 v53, v46, v49
	s_waitcnt vmcnt(1) lgkmcnt(2)
	v_mul_f32_e32 v37, v58, v37
	v_cndmask_b32_e64 v37, v37, -v37, s[6:7]
	s_waitcnt vmcnt(0)
	v_fmac_f32_e32 v37, v62, v11
	s_waitcnt lgkmcnt(1)
	v_mul_f32_e32 v11, v59, v52
	v_cndmask_b32_e64 v11, v11, -v11, s[6:7]
	v_mul_f32_e32 v8, v70, v8
	v_fmac_f32_e32 v11, v63, v36
	s_waitcnt lgkmcnt(0)
	v_mul_f32_e32 v36, v60, v53
	v_mul_f32_e32 v50, s25, v50
	v_mul_f32_e32 v9, s25, v9
	v_mul_f32_e32 v8, v3, v8
	v_cndmask_b32_e64 v36, v36, -v36, s[6:7]
	v_med3_f32 v50, v50, s2, v40
	v_med3_f32 v9, v9, s2, v40
	v_mov_b32_e32 v52, v15
	v_cndmask_b32_e64 v33, v33, -v33, s[6:7]
	v_fmac_f32_e32 v36, v64, v49
	ds_bpermute_b32 v49, v46, v8
	v_cvt_pk_fp8_f32 v52, v50, v9
	v_fmac_f32_e32 v33, v57, v66
	v_mul_f32_e32 v9, s25, v51
	v_mul_f32_e32 v33, s25, v33
	v_med3_f32 v9, v9, s2, v40
	v_med3_f32 v33, v33, s2, v40
	v_cvt_pk_fp8_f32 v52, v9, v33 op_sel:[0,0,1]
	v_mul_f32_e32 v37, s25, v37
	v_mul_f32_e32 v11, s25, v11
	s_waitcnt lgkmcnt(0)
	v_mul_f32_e32 v9, v61, v49
	v_med3_f32 v37, v37, s2, v40
	v_med3_f32 v11, v11, s2, v40
	v_mov_b32_e32 v50, v15
	v_cndmask_b32_e64 v9, v9, -v9, s[6:7]
	v_cvt_pk_fp8_f32 v50, v37, v11
	v_fmac_f32_e32 v9, v65, v8
	v_lshrrev_b32_e32 v33, 2, v52
	v_mul_f32_e32 v11, s25, v36
	v_mul_f32_e32 v9, s25, v9
	v_and_b32_e32 v8, 0x1f1f1f1f, v52
	v_and_b32_e32 v33, 0x20202020, v33
	v_med3_f32 v11, v11, s2, v40
	v_med3_f32 v9, v9, s2, v40
	v_or_b32_e32 v49, v33, v8
	v_cvt_pk_fp8_f32 v50, v11, v9 op_sel:[0,0,1]
	v_bitop3_b32 v8, v33, 63, v8 bitop3:0xc8
	v_lshrrev_b32_e32 v33, 2, v49
	v_and_or_b32 v8, v33, s13, v8
	v_lshrrev_b32_e32 v33, 4, v49
	v_lshrrev_b32_e32 v9, 6, v49
	v_and_b32_e32 v33, 0x3f000, v33
	v_and_b32_e32 v9, 0xfc0000, v9
	v_or3_b32 v8, v8, v33, v9
	v_and_b32_e32 v9, 0x1f1f1f1f, v50
	v_lshrrev_b32_e32 v11, 2, v50
	v_and_or_b32 v9, v11, s3, v9
	v_lshrrev_b32_e32 v11, 2, v9
	v_and_b32_e32 v11, 0xfc0, v11
	v_or_b32_e32 v33, v11, v9
	v_lshrrev_b32_e32 v36, 4, v9
	v_lshrrev_b32_e32 v9, 6, v9
	v_and_b32_e32 v36, 0x3f000, v36
	v_and_b32_e32 v9, 0xfc0000, v9
	v_or3_b32 v9, v36, v9, v11
	v_lshl_or_b32 v8, v33, 24, v8
	v_lshrrev_b32_e32 v9, 8, v9
	v_mov_b32_e32 v33, v15
	v_mov_b32_e32 v36, v15
	s_nop 0
	v_mov_b32_dpp v33, v8 quad_perm:[1,0,3,2] row_mask:0xf bank_mask:0xf
	v_mov_b32_dpp v36, v9 quad_perm:[1,0,3,2] row_mask:0xf bank_mask:0xf
	s_and_saveexec_b64 s[10:11], s[8:9]
	s_cbranch_execz .LBB0_310
	v_ashrrev_i32_e32 v11, 31, v10
	v_lshlrev_b64 v[10:11], 7, v[10:11]
	v_lshl_add_u64 v[50:51], v[30:31], 0, v[10:11]
	v_lshl_or_b32 v9, v33, 16, v9
	v_perm_b32 v10, v33, v36, s15
	global_store_dword v[50:51], v8, off
	v_lshl_add_u64 v[204:205], v[50:51], 0, v[202:203]
	global_store_dword v[204:205], v9, off offset:4
	global_store_dword v[204:205], v10, off offset:8
.LBB0_310:
	s_or_b64 exec, exec, s[10:11]
	v_cvt_f32_fp8_sdwa v33, v34 src0_sel:BYTE_1
	v_cvt_f32_fp8_e32 v11, v34
	v_cvt_f32_fp8_sdwa v49, v34 src0_sel:BYTE_2
	v_cvt_f32_fp8_sdwa v64, v34 src0_sel:BYTE_3
	v_cvt_f32_fp8_e32 v65, v35
	v_mul_f32_e32 v54, v33, v33
	v_add_u32_e32 v10, 8, v32
	v_cvt_f32_fp8_sdwa v66, v35 src0_sel:BYTE_1
	v_fmac_f32_e32 v54, v11, v11
	v_and_b32_e32 v8, 63, v10
	v_bfe_u32 v9, v10, 6, 8
	v_cvt_f32_fp8_sdwa v67, v35 src0_sel:BYTE_2
	v_fmac_f32_e32 v54, v49, v49
	v_cndmask_b32_e64 v8, v8, v9, s[4:5]
	v_cvt_f32_fp8_sdwa v68, v35 src0_sel:BYTE_3
	v_fmac_f32_e32 v54, v64, v64
	v_lshlrev_b32_e32 v8, 7, v8
	v_mov_b32_e32 v9, v15
	v_fmac_f32_e32 v54, v65, v65
	v_lshl_add_u64 v[8:9], v[20:21], 0, v[8:9]
	v_fmac_f32_e32 v54, v66, v66
	v_lshl_add_u64 v[62:63], v[8:9], 0, v[14:15]
	v_fmac_f32_e32 v54, v67, v67
	global_load_dwordx4 v[34:37], v[62:63], off
	global_load_dwordx4 v[50:53], v[8:9], off
	v_fmac_f32_e32 v54, v68, v68
	ds_bpermute_b32 v55, v45, v54
	s_waitcnt lgkmcnt(0)
	v_add_f32_e32 v54, v54, v55
	ds_bpermute_b32 v55, v47, v54
	s_waitcnt lgkmcnt(0)
	v_add_f32_e32 v69, v54, v55
	global_load_dwordx4 v[54:57], v[62:63], off offset:16
	global_load_dwordx4 v[58:61], v[8:9], off offset:16
	ds_bpermute_b32 v70, v46, v69
	s_waitcnt lgkmcnt(0)
	v_add_f32_e32 v8, v69, v70
	ds_bpermute_b32 v9, v48, v8
	s_waitcnt lgkmcnt(0)
	v_add_f32_e32 v8, v8, v9
	v_fmamk_f32 v8, v8, 0x3c000000, v38
	v_rsq_f32_e32 v8, v8
	s_nop 0
	v_mul_f32_e32 v9, v11, v8
	v_mul_f32_e32 v9, v4, v9
	v_mul_f32_e32 v11, v65, v8
	v_mul_f32_e32 v33, v33, v8
	ds_bpermute_b32 v65, v46, v9
	v_mul_f32_e32 v33, v5, v33
	v_mul_f32_e32 v62, v66, v8
	ds_bpermute_b32 v66, v46, v33
	v_mul_f32_e32 v49, v49, v8
	v_mul_f32_e32 v49, v6, v49
	s_waitcnt vmcnt(3) lgkmcnt(1)
	v_mul_f32_e32 v34, v34, v65
	v_cndmask_b32_e64 v34, v34, -v34, s[6:7]
	v_mul_f32_e32 v63, v67, v8
	v_mul_f32_e32 v64, v64, v8
	ds_bpermute_b32 v67, v46, v49
	s_waitcnt vmcnt(2)
	v_fmac_f32_e32 v34, v50, v9
	s_waitcnt lgkmcnt(1)
	v_mul_f32_e32 v9, v35, v66
	v_mul_f32_e32 v64, v7, v64
	v_cndmask_b32_e64 v9, v9, -v9, s[6:7]
	v_fmac_f32_e32 v9, v51, v33
	ds_bpermute_b32 v33, v46, v64
	v_mul_f32_e32 v11, v0, v11
	s_waitcnt lgkmcnt(1)
	v_mul_f32_e32 v35, v36, v67
	ds_bpermute_b32 v36, v46, v11
	v_mul_f32_e32 v62, v1, v62
	v_mul_f32_e32 v63, v2, v63
	v_cndmask_b32_e64 v35, v35, -v35, s[6:7]
	v_fmac_f32_e32 v35, v52, v49
	s_waitcnt lgkmcnt(1)
	v_mul_f32_e32 v33, v37, v33
	ds_bpermute_b32 v37, v46, v62
	ds_bpermute_b32 v49, v46, v63
	v_mul_f32_e32 v8, v68, v8
	s_waitcnt vmcnt(1) lgkmcnt(2)
	v_mul_f32_e32 v36, v54, v36
	v_mul_f32_e32 v34, s25, v34
	v_mul_f32_e32 v9, s25, v9
	v_mul_f32_e32 v8, v3, v8
	v_cndmask_b32_e64 v36, v36, -v36, s[6:7]
	v_med3_f32 v34, v34, s2, v40
	v_med3_f32 v9, v9, s2, v40
	v_mov_b32_e32 v50, v15
	v_cndmask_b32_e64 v33, v33, -v33, s[6:7]
	s_waitcnt vmcnt(0)
	v_fmac_f32_e32 v36, v58, v11
	s_waitcnt lgkmcnt(1)
	v_mul_f32_e32 v11, v55, v37
	s_waitcnt lgkmcnt(0)
	v_mul_f32_e32 v37, v56, v49
	ds_bpermute_b32 v49, v46, v8
	v_cvt_pk_fp8_f32 v50, v34, v9
	v_fmac_f32_e32 v33, v53, v64
	v_cndmask_b32_e64 v11, v11, -v11, s[6:7]
	v_mul_f32_e32 v9, s25, v35
	v_mul_f32_e32 v33, s25, v33
	v_fmac_f32_e32 v11, v59, v62
	v_med3_f32 v9, v9, s2, v40
	v_med3_f32 v33, v33, s2, v40
	v_cvt_pk_fp8_f32 v50, v9, v33 op_sel:[0,0,1]
	v_mul_f32_e32 v35, s25, v36
	v_mul_f32_e32 v11, s25, v11
	s_waitcnt lgkmcnt(0)
	v_mul_f32_e32 v9, v57, v49
	v_med3_f32 v35, v35, s2, v40
	v_med3_f32 v11, v11, s2, v40
	v_mov_b32_e32 v36, v15
	v_cndmask_b32_e64 v37, v37, -v37, s[6:7]
	v_cndmask_b32_e64 v9, v9, -v9, s[6:7]
	v_cvt_pk_fp8_f32 v36, v35, v11
	v_fmac_f32_e32 v37, v60, v63
	v_fmac_f32_e32 v9, v61, v8
	v_lshrrev_b32_e32 v33, 2, v50
	v_mul_f32_e32 v11, s25, v37
	v_mul_f32_e32 v9, s25, v9
	v_and_b32_e32 v8, 0x1f1f1f1f, v50
	v_and_b32_e32 v33, 0x20202020, v33
	v_med3_f32 v11, v11, s2, v40
	v_med3_f32 v9, v9, s2, v40
	v_or_b32_e32 v34, v33, v8
	v_cvt_pk_fp8_f32 v36, v11, v9 op_sel:[0,0,1]
	v_bitop3_b32 v8, v33, 63, v8 bitop3:0xc8
	v_lshrrev_b32_e32 v33, 2, v34
	v_and_or_b32 v8, v33, s13, v8
	v_lshrrev_b32_e32 v33, 4, v34
	v_lshrrev_b32_e32 v9, 6, v34
	v_and_b32_e32 v33, 0x3f000, v33
	v_and_b32_e32 v9, 0xfc0000, v9
	v_or3_b32 v8, v8, v33, v9
	v_and_b32_e32 v9, 0x1f1f1f1f, v36
	v_lshrrev_b32_e32 v11, 2, v36
	v_and_or_b32 v9, v11, s3, v9
	v_lshrrev_b32_e32 v11, 2, v9
	v_and_b32_e32 v11, 0xfc0, v11
	v_or_b32_e32 v33, v11, v9
	v_lshrrev_b32_e32 v34, 4, v9
	v_lshrrev_b32_e32 v9, 6, v9
	v_and_b32_e32 v34, 0x3f000, v34
	v_and_b32_e32 v9, 0xfc0000, v9
	v_or3_b32 v9, v34, v9, v11
	v_lshl_or_b32 v8, v33, 24, v8
	v_lshrrev_b32_e32 v9, 8, v9
	v_mov_b32_e32 v33, v15
	v_mov_b32_e32 v34, v15
	s_nop 0
	v_mov_b32_dpp v33, v8 quad_perm:[1,0,3,2] row_mask:0xf bank_mask:0xf
	v_mov_b32_dpp v34, v9 quad_perm:[1,0,3,2] row_mask:0xf bank_mask:0xf
	s_and_saveexec_b64 s[10:11], s[8:9]
	s_cbranch_execz .LBB0_312
	v_ashrrev_i32_e32 v11, 31, v10
	v_lshlrev_b64 v[10:11], 7, v[10:11]
	v_lshl_add_u64 v[36:37], v[30:31], 0, v[10:11]
	v_lshl_or_b32 v9, v33, 16, v9
	v_perm_b32 v10, v33, v34, s15
	global_store_dword v[36:37], v8, off
	v_lshl_add_u64 v[204:205], v[36:37], 0, v[202:203]
	global_store_dword v[204:205], v9, off offset:4
	global_store_dword v[204:205], v10, off offset:8
.LBB0_312:
	s_or_b64 exec, exec, s[10:11]
	s_nop 0
	v_add_u32_e32 v8, 12, v32
	v_and_b32_e32 v10, 63, v8
	v_bfe_u32 v11, v8, 6, 8
	v_cndmask_b32_e64 v10, v10, v11, s[4:5]
	v_lshlrev_b32_e32 v10, 7, v10
	v_mov_b32_e32 v11, v15
	v_cvt_f32_fp8_sdwa v49, v44 src0_sel:BYTE_1
	v_lshl_add_u64 v[10:11], v[20:21], 0, v[10:11]
	v_cvt_f32_fp8_e32 v9, v44
	v_lshl_add_u64 v[36:37], v[10:11], 0, v[14:15]
	v_cvt_f32_fp8_sdwa v62, v44 src0_sel:BYTE_2
	global_load_dwordx4 v[32:35], v[36:37], off
	global_load_dwordx4 v[50:53], v[10:11], off
	v_cvt_f32_fp8_sdwa v44, v44 src0_sel:BYTE_3
	v_cvt_f32_fp8_e32 v63, v43
	v_mul_f32_e32 v54, v49, v49
	v_cvt_f32_fp8_sdwa v64, v43 src0_sel:BYTE_1
	v_fmac_f32_e32 v54, v9, v9
	v_cvt_f32_fp8_sdwa v65, v43 src0_sel:BYTE_2
	v_fmac_f32_e32 v54, v62, v62
	v_cvt_f32_fp8_sdwa v43, v43 src0_sel:BYTE_3
	v_fmac_f32_e32 v54, v44, v44
	v_fmac_f32_e32 v54, v63, v63
	v_fmac_f32_e32 v54, v64, v64
	v_fmac_f32_e32 v54, v65, v65
	v_fmac_f32_e32 v54, v43, v43
	ds_bpermute_b32 v45, v45, v54
	s_waitcnt lgkmcnt(0)
	v_add_f32_e32 v45, v54, v45
	global_load_dwordx4 v[54:57], v[36:37], off offset:16
	global_load_dwordx4 v[58:61], v[10:11], off offset:16
	ds_bpermute_b32 v47, v47, v45
	s_waitcnt lgkmcnt(0)
	v_add_f32_e32 v45, v45, v47
	ds_bpermute_b32 v47, v46, v45
	s_waitcnt lgkmcnt(0)
	v_add_f32_e32 v10, v45, v47
	ds_bpermute_b32 v11, v48, v10
	s_waitcnt lgkmcnt(0)
	v_add_f32_e32 v10, v10, v11
	v_fmamk_f32 v10, v10, 0x3c000000, v38
	v_rsq_f32_e32 v10, v10
	s_nop 0
	v_mul_f32_e32 v9, v9, v10
	v_mul_f32_e32 v4, v4, v9
	v_mul_f32_e32 v36, v49, v10
	ds_bpermute_b32 v9, v46, v4
	v_mul_f32_e32 v11, v63, v10
	v_mul_f32_e32 v37, v64, v10
	v_mul_f32_e32 v45, v62, v10
	v_mul_f32_e32 v47, v65, v10
	v_mul_f32_e32 v44, v44, v10
	v_mul_f32_e32 v10, v43, v10
	v_mul_f32_e32 v5, v5, v36
	v_mul_f32_e32 v3, v3, v10
	ds_bpermute_b32 v10, v46, v5
	s_waitcnt vmcnt(3) lgkmcnt(1)
	v_mul_f32_e32 v9, v32, v9
	v_mul_f32_e32 v6, v6, v45
	v_cndmask_b32_e64 v9, v9, -v9, s[6:7]
	v_mul_f32_e32 v0, v0, v11
	ds_bpermute_b32 v11, v46, v6
	s_waitcnt vmcnt(2)
	v_fmac_f32_e32 v9, v50, v4
	s_waitcnt lgkmcnt(1)
	v_mul_f32_e32 v4, v33, v10
	v_mul_f32_e32 v7, v7, v44
	v_cndmask_b32_e64 v4, v4, -v4, s[6:7]
	v_fmac_f32_e32 v4, v51, v5
	ds_bpermute_b32 v5, v46, v7
	s_waitcnt lgkmcnt(1)
	v_mul_f32_e32 v10, v34, v11
	v_cndmask_b32_e64 v10, v10, -v10, s[6:7]
	v_fmac_f32_e32 v10, v52, v6
	ds_bpermute_b32 v6, v46, v0
	s_waitcnt lgkmcnt(1)
	v_mul_f32_e32 v5, v35, v5
	v_mul_f32_e32 v1, v1, v37
	v_cndmask_b32_e64 v5, v5, -v5, s[6:7]
	v_fmac_f32_e32 v5, v53, v7
	ds_bpermute_b32 v7, v46, v1
	v_mul_f32_e32 v2, v2, v47
	ds_bpermute_b32 v11, v46, v2
	s_waitcnt vmcnt(1) lgkmcnt(2)
	v_mul_f32_e32 v6, v54, v6
	v_cndmask_b32_e64 v6, v6, -v6, s[6:7]
	s_waitcnt vmcnt(0)
	v_fmac_f32_e32 v6, v58, v0
	s_waitcnt lgkmcnt(1)
	v_mul_f32_e32 v0, v55, v7
	v_cndmask_b32_e64 v0, v0, -v0, s[6:7]
	v_fmac_f32_e32 v0, v59, v1
	s_waitcnt lgkmcnt(0)
	v_mul_f32_e32 v1, v56, v11
	v_cndmask_b32_e64 v1, v1, -v1, s[6:7]
	v_fmac_f32_e32 v1, v60, v2
	ds_bpermute_b32 v2, v46, v3
	v_mul_f32_e32 v7, s25, v9
	v_mul_f32_e32 v4, s25, v4
	v_med3_f32 v7, v7, s2, v40
	v_med3_f32 v4, v4, s2, v40
	v_mov_b32_e32 v9, v15
	v_cvt_pk_fp8_f32 v9, v7, v4
	v_mul_f32_e32 v6, s25, v6
	v_mul_f32_e32 v0, s25, v0
	s_waitcnt lgkmcnt(0)
	v_mul_f32_e32 v2, v57, v2
	v_med3_f32 v6, v6, s2, v40
	v_med3_f32 v0, v0, s2, v40
	v_mov_b32_e32 v7, v15
	v_mul_f32_e32 v4, s25, v10
	v_mul_f32_e32 v5, s25, v5
	v_cndmask_b32_e64 v2, v2, -v2, s[6:7]
	v_cvt_pk_fp8_f32 v7, v6, v0
	v_med3_f32 v4, v4, s2, v40
	v_med3_f32 v5, v5, s2, v40
	v_fmac_f32_e32 v2, v61, v3
	v_cvt_pk_fp8_f32 v9, v4, v5 op_sel:[0,0,1]
	v_mul_f32_e32 v0, s25, v1
	v_mul_f32_e32 v1, s25, v2
	v_med3_f32 v0, v0, s2, v40
	v_med3_f32 v1, v1, s2, v40
	v_cvt_pk_fp8_f32 v7, v0, v1 op_sel:[0,0,1]
	v_lshrrev_b32_e32 v4, 2, v9
	v_and_b32_e32 v3, 0x1f1f1f1f, v9
	v_and_b32_e32 v4, 0x20202020, v4
	v_or_b32_e32 v5, v4, v3
	v_and_b32_e32 v1, 0x1f1f1f1f, v7
	v_lshrrev_b32_e32 v2, 2, v7
	v_bitop3_b32 v3, v4, 63, v3 bitop3:0xc8
	v_lshrrev_b32_e32 v4, 2, v5
	v_and_or_b32 v1, v2, s3, v1
	v_and_or_b32 v3, v4, s13, v3
	v_lshrrev_b32_e32 v4, 4, v5
	v_lshrrev_b32_e32 v0, 6, v5
	v_lshrrev_b32_e32 v2, 2, v1
	v_and_b32_e32 v4, 0x3f000, v4
	v_and_b32_e32 v0, 0xfc0000, v0
	v_and_b32_e32 v2, 0xfc0, v2
	v_or3_b32 v0, v3, v4, v0
	v_or_b32_e32 v3, v2, v1
	v_lshrrev_b32_e32 v4, 4, v1
	v_lshrrev_b32_e32 v1, 6, v1
	v_and_b32_e32 v4, 0x3f000, v4
	v_and_b32_e32 v1, 0xfc0000, v1
	v_or3_b32 v1, v4, v1, v2
	v_lshl_or_b32 v0, v3, 24, v0
	v_lshrrev_b32_e32 v1, 8, v1
	v_mov_b32_e32 v2, v15
	v_mov_b32_e32 v3, v15
	s_nop 0
	v_mov_b32_dpp v2, v0 quad_perm:[1,0,3,2] row_mask:0xf bank_mask:0xf
	v_mov_b32_dpp v3, v1 quad_perm:[1,0,3,2] row_mask:0xf bank_mask:0xf
	s_and_saveexec_b64 s[10:11], s[8:9]
	s_cbranch_execz .LBB0_298
	v_ashrrev_i32_e32 v9, 31, v8
	v_lshlrev_b64 v[4:5], 7, v[8:9]
	v_lshl_add_u64 v[4:5], v[30:31], 0, v[4:5]
	v_lshl_or_b32 v1, v2, 16, v1
	v_perm_b32 v2, v2, v3, s15
	global_store_dword v[4:5], v0, off
	v_lshl_add_u64 v[204:205], v[4:5], 0, v[202:203]
	global_store_dword v[204:205], v1, off offset:4
	global_store_dword v[204:205], v2, off offset:8
	s_branch .LBB0_298

.LBB0_973:
	s_waitcnt vmcnt(15)
	v_and_b32_e32 v203, 0xffff0000, v133
	v_and_b32_e32 v201, 0xffff0000, v132
	v_lshlrev_b32_e32 v202, 16, v133
	v_mul_f32_e32 v130, v203, v203
	v_lshlrev_b32_e32 v200, 16, v132
	v_pk_fma_f32 v[168:169], v[202:203], v[202:203], v[130:131] op_sel_hi:[1,1,0]
	s_waitcnt vmcnt(14)
	v_and_b32_e32 v207, 0xffff0000, v135
	v_and_b32_e32 v206, 0xffff0000, v134
	v_mul_f32_e32 v130, v201, v201
	v_lshlrev_b32_e32 v205, 16, v135
	v_lshlrev_b32_e32 v204, 16, v134
	v_pk_mul_f32 v[170:171], v[206:207], v[206:207]
	s_waitcnt vmcnt(12)
	v_lshlrev_b32_e32 v213, 16, v144
	v_pk_fma_f32 v[172:173], v[200:201], v[200:201], v[130:131] op_sel_hi:[1,1,0]
	v_pk_fma_f32 v[170:171], v[204:205], v[204:205], v[170:171]
	v_and_b32_e32 v215, 0xffff0000, v144
	v_mov_b32_e32 v212, v172
	v_mov_b32_e32 v174, v168
	s_waitcnt lgkmcnt(0)
	v_mov_b32_e32 v175, v213
	v_and_b32_e32 v209, 0xffff0000, v140
	v_mul_f32_e32 v129, v215, v215
	v_pk_add_f32 v[168:169], v[172:173], v[168:169]
	v_pk_mul_f32 v[172:173], v[212:213], v[174:175]
	v_pk_add_f32 v[170:171], v[170:171], v[170:171] op_sel:[0,1] op_sel_hi:[1,0]
	v_lshlrev_b32_e32 v208, 16, v140
	v_and_b32_e32 v211, 0xffff0000, v141
	v_mov_b32_e32 v169, v173
	v_mov_b32_e32 v171, v129
	v_mul_f32_e32 v130, v209, v209
	v_lshlrev_b32_e32 v210, 16, v141
	v_lshlrev_b32_e32 v216, 16, v145
	v_and_b32_e32 v217, 0xffff0000, v145
	v_pk_add_f32 v[168:169], v[168:169], v[170:171]
	v_pk_fma_f32 v[170:171], v[208:209], v[208:209], v[130:131] op_sel_hi:[1,1,0]
	v_mul_f32_e32 v130, v211, v211
	v_mul_f32_e32 v176, v216, v216
	v_mul_f32_e32 v177, v217, v217
	v_pk_fma_f32 v[172:173], v[210:211], v[210:211], v[130:131] op_sel_hi:[1,1,0]
	v_mov_b32_e32 v171, v176
	v_mov_b32_e32 v173, v177
	v_pk_add_f32 v[170:171], v[170:171], v[172:173]
	s_waitcnt vmcnt(7)
	v_and_b32_e32 v221, 0xffff0000, v151
	v_and_b32_e32 v220, 0xffff0000, v150
	v_pk_add_f32 v[218:219], v[168:169], v[170:171]
	v_lshlrev_b32_e32 v177, 16, v151
	v_lshlrev_b32_e32 v176, 16, v150
	v_pk_mul_f32 v[168:169], v[220:221], v[220:221]
	s_waitcnt vmcnt(6)
	v_and_b32_e32 v181, 0xffff0000, v153
	v_pk_fma_f32 v[168:169], v[176:177], v[176:177], v[168:169]
	v_and_b32_e32 v180, 0xffff0000, v152
	v_pk_add_f32 v[222:223], v[168:169], v[168:169] op_sel:[0,1] op_sel_hi:[1,0]
	s_waitcnt vmcnt(4)
	v_lshlrev_b32_e32 v175, 16, v162
	v_pk_add_f32 v[218:219], v[218:219], v[218:219] op_sel:[0,1] op_sel_hi:[1,0]
	v_lshlrev_b32_e32 v183, 16, v153
	v_lshlrev_b32_e32 v182, 16, v152
	v_pk_mul_f32 v[168:169], v[180:181], v[180:181]
	v_mov_b32_e32 v174, v218
	v_mov_b32_e32 v226, v222
	v_mov_b32_e32 v227, v175
	v_pk_fma_f32 v[224:225], v[182:183], v[182:183], v[168:169]
	v_and_b32_e32 v173, 0xffff0000, v162
	v_pk_add_f32 v[218:219], v[218:219], v[222:223]
	v_pk_mul_f32 v[222:223], v[174:175], v[226:227]
	v_and_b32_e32 v171, 0xffff0000, v156
	v_mul_f32_e32 v129, v173, v173
	v_mov_b32_e32 v219, v223
	v_pk_add_f32 v[222:223], v[224:225], v[224:225] op_sel:[0,1] op_sel_hi:[1,0]
	v_lshlrev_b32_e32 v170, 16, v156
	v_and_b32_e32 v179, 0xffff0000, v157
	v_mov_b32_e32 v223, v129
	v_mul_f32_e32 v130, v171, v171
	v_lshlrev_b32_e32 v178, 16, v157
	v_lshlrev_b32_e32 v168, 16, v163
	v_and_b32_e32 v169, 0xffff0000, v163
	v_pk_add_f32 v[218:219], v[218:219], v[222:223]
	v_pk_fma_f32 v[222:223], v[170:171], v[170:171], v[130:131] op_sel_hi:[1,1,0]
	v_mul_f32_e32 v130, v179, v179
	v_mul_f32_e32 v172, v168, v168
	v_mul_f32_e32 v212, v169, v169
	v_pk_fma_f32 v[224:225], v[178:179], v[178:179], v[130:131] op_sel_hi:[1,1,0]
	v_mov_b32_e32 v223, v172
	v_mov_b32_e32 v225, v212
	v_pk_add_f32 v[222:223], v[222:223], v[224:225]
	s_nop 0
	v_pk_add_f32 v[218:219], v[218:219], v[222:223]
	s_barrier
	v_add_f32_e32 v129, v218, v219
	ds_bpermute_b32 v130, v184, v129
	v_mov_b32_e32 v218, v205
	v_mov_b32_e32 v205, v206
	v_mov_b32_e32 v219, v207
	s_waitcnt lgkmcnt(0)
	v_add_f32_e32 v129, v129, v130
	ds_bpermute_b32 v130, v185, v129
	v_and_b32_e32 v223, 0xffff0000, v142
	v_lshlrev_b32_e32 v224, 16, v143
	v_and_b32_e32 v225, 0xffff0000, v143
	v_mul_f32_e32 v222, v225, v225
	s_waitcnt lgkmcnt(0)
	v_add_f32_e32 v129, v129, v130
	ds_bpermute_b32 v130, v186, v129
	v_and_b32_e32 v229, 0xffff0000, v147
	v_and_b32_e32 v228, 0xffff0000, v146
	s_waitcnt vmcnt(2)
	v_and_b32_e32 v233, 0xffff0000, v155
	v_and_b32_e32 v232, 0xffff0000, v154
	s_waitcnt lgkmcnt(0)
	v_add_f32_e32 v129, v129, v130
	ds_bpermute_b32 v130, v187, v129
	s_waitcnt vmcnt(0)
	v_lshlrev_b32_e32 v239, 16, v160
	v_lshlrev_b32_e32 v231, 16, v155
	v_lshlrev_b32_e32 v230, 16, v154
	v_mov_b32_e32 v245, v239
	s_waitcnt lgkmcnt(0)
	v_add_f32_e32 v129, v129, v130
	ds_bpermute_b32 v130, v188, v129
	v_and_b32_e32 v241, 0xffff0000, v160
	v_and_b32_e32 v235, 0xffff0000, v158
	v_lshlrev_b32_e32 v234, 16, v158
	v_and_b32_e32 v237, 0xffff0000, v159
	s_waitcnt lgkmcnt(0)
	v_add_f32_e32 v129, v129, v130
	ds_bpermute_b32 v130, v189, v129
	v_lshlrev_b32_e32 v236, 16, v159
	v_lshlrev_b32_e32 v242, 16, v161
	v_and_b32_e32 v243, 0xffff0000, v161
	v_mov_b32_e32 v240, v239
	s_waitcnt lgkmcnt(0)
	v_add_f32_e32 v129, v129, v130
	v_fmamk_f32 v129, v129, 0x3a000000, v193
	v_rsq_f32_e32 v130, v129
	s_nop 0
	s_add_i32 s30, s30, s74
	s_cmpk_gt_i32 s30, 0x7ff
	s_cselect_b64 s[34:35], -1, 0
	v_pk_mul_f32 v[204:205], v[130:131], v[204:205] op_sel_hi:[0,1]
	v_mov_b32_e32 v172, 0
	v_cvt_pk_fp8_f32 v172, v204, v205
	v_pk_mul_f32 v[200:201], v[130:131], v[200:201] op_sel_hi:[0,1]
	v_mov_b32_e32 v129, 0
	v_pk_mul_f32 v[206:207], v[130:131], v[218:219] op_sel_hi:[0,1]
	v_cvt_pk_fp8_f32 v129, v200, v201
	v_cvt_pk_fp8_f32 v172, v206, v207 op_sel:[0,0,1]
	v_pk_mul_f32 v[202:203], v[130:131], v[202:203] op_sel_hi:[0,1]
	v_mov_b32_e32 v214, v213
	v_cvt_pk_fp8_f32 v129, v202, v203 op_sel:[0,0,1]
	ds_write_b128 v195, v[200:203]
	global_store_dword v[166:167], v172, off offset:-1792
	v_pk_mul_f32 v[200:201], v[130:131], v[208:209] op_sel_hi:[0,1]
	v_pk_mul_f32 v[208:209], v[214:215], v[130:131] op_sel_hi:[1,0]
	v_mov_b32_e32 v172, 0
	v_cvt_pk_fp8_f32 v172, v208, v209
	global_store_dword v[166:167], v129, off offset:-2048
	v_mov_b32_e32 v129, 0
	v_pk_mul_f32 v[202:203], v[130:131], v[210:211] op_sel_hi:[0,1]
	v_pk_mul_f32 v[210:211], v[216:217], v[130:131] op_sel_hi:[1,0]
	v_cvt_pk_fp8_f32 v129, v200, v201
	v_cvt_pk_fp8_f32 v172, v210, v211 op_sel:[0,0,1]
	ds_write_b128 v195, v[208:211] offset:3072
	v_and_b32_e32 v211, 0xffff0000, v149
	v_cvt_pk_fp8_f32 v129, v202, v203 op_sel:[0,0,1]
	ds_write_b128 v195, v[200:203] offset:2048
	global_store_dword v[166:167], v172, off offset:-1280
	v_mov_b32_e32 v200, v177
	v_mov_b32_e32 v201, v221
	v_and_b32_e32 v209, 0xffff0000, v148
	v_lshlrev_b32_e32 v210, 16, v149
	v_mul_f32_e32 v172, v211, v211
	v_pk_mul_f32 v[202:203], v[130:131], v[200:201] op_sel_hi:[0,1]
	v_lshlrev_b32_e32 v208, 16, v148
	v_pk_fma_f32 v[200:201], v[210:211], v[210:211], v[172:173] op_sel_hi:[1,1,0]
	v_and_b32_e32 v215, 0xffff0000, v137
	v_and_b32_e32 v214, 0xffff0000, v136
	v_mul_f32_e32 v172, v209, v209
	ds_write_b128 v195, v[204:207] offset:1024
	v_lshlrev_b32_e32 v213, 16, v137
	v_lshlrev_b32_e32 v212, 16, v136
	v_pk_mul_f32 v[204:205], v[214:215], v[214:215]
	v_lshlrev_b32_e32 v221, 16, v142
	v_pk_fma_f32 v[206:207], v[208:209], v[208:209], v[172:173] op_sel_hi:[1,1,0]
	v_mov_b32_e32 v177, v220
	v_pk_fma_f32 v[204:205], v[212:213], v[212:213], v[204:205]
	v_mov_b32_e32 v220, v206
	v_mov_b32_e32 v226, v200
	v_mov_b32_e32 v227, v221
	global_store_dword v[166:167], v129, off offset:-1536
	v_and_b32_e32 v217, 0xffff0000, v138
	v_mul_f32_e32 v129, v223, v223
	v_pk_add_f32 v[200:201], v[206:207], v[200:201]
	v_pk_mul_f32 v[206:207], v[220:221], v[226:227]
	v_pk_add_f32 v[204:205], v[204:205], v[204:205] op_sel:[0,1] op_sel_hi:[1,0]
	v_lshlrev_b32_e32 v216, 16, v138
	v_and_b32_e32 v219, 0xffff0000, v139
	v_mov_b32_e32 v201, v207
	v_mov_b32_e32 v205, v129
	v_mul_f32_e32 v172, v217, v217
	v_lshlrev_b32_e32 v218, 16, v139
	v_pk_add_f32 v[200:201], v[200:201], v[204:205]
	v_pk_fma_f32 v[204:205], v[216:217], v[216:217], v[172:173] op_sel_hi:[1,1,0]
	v_mul_f32_e32 v172, v219, v219
	v_mul_f32_e32 v174, v224, v224
	v_pk_fma_f32 v[206:207], v[218:219], v[218:219], v[172:173] op_sel_hi:[1,1,0]
	v_mov_b32_e32 v205, v174
	v_mov_b32_e32 v207, v222
	v_pk_add_f32 v[204:205], v[204:205], v[206:207]
	v_lshlrev_b32_e32 v227, 16, v147
	v_pk_add_f32 v[200:201], v[200:201], v[204:205]
	v_lshlrev_b32_e32 v226, 16, v146
	v_pk_mul_f32 v[204:205], v[228:229], v[228:229]
	v_pk_add_f32 v[200:201], v[200:201], v[200:201] op_sel:[0,1] op_sel_hi:[1,0]
	v_pk_fma_f32 v[204:205], v[226:227], v[226:227], v[204:205]
	v_pk_mul_f32 v[206:207], v[232:233], v[232:233]
	v_pk_add_f32 v[204:205], v[204:205], v[204:205] op_sel:[0,1] op_sel_hi:[1,0]
	v_mov_b32_e32 v238, v200
	v_mov_b32_e32 v244, v204
	v_pk_fma_f32 v[206:207], v[230:231], v[230:231], v[206:207]
	v_pk_add_f32 v[200:201], v[200:201], v[204:205]
	v_pk_mul_f32 v[204:205], v[238:239], v[244:245]
	v_mul_f32_e32 v129, v241, v241
	v_mov_b32_e32 v201, v205
	v_pk_add_f32 v[204:205], v[206:207], v[206:207] op_sel:[0,1] op_sel_hi:[1,0]
	v_mul_f32_e32 v172, v235, v235
	v_mov_b32_e32 v205, v129
	v_pk_add_f32 v[200:201], v[200:201], v[204:205]
	v_pk_fma_f32 v[204:205], v[234:235], v[234:235], v[172:173] op_sel_hi:[1,1,0]
	v_mul_f32_e32 v172, v237, v237
	v_mul_f32_e32 v174, v242, v242
	v_mul_f32_e32 v220, v243, v243
	v_pk_fma_f32 v[206:207], v[236:237], v[236:237], v[172:173] op_sel_hi:[1,1,0]
	v_mov_b32_e32 v205, v174
	v_mov_b32_e32 v207, v220
	v_pk_add_f32 v[204:205], v[204:205], v[206:207]
	v_mov_b32_e32 v174, 0
	v_pk_add_f32 v[200:201], v[200:201], v[204:205]
	v_pk_mul_f32 v[178:179], v[130:131], v[178:179] op_sel_hi:[0,1]
	v_add_f32_e32 v129, v200, v201
	ds_bpermute_b32 v172, v184, v129
	v_pk_mul_f32 v[200:201], v[130:131], v[176:177] op_sel_hi:[0,1]
	v_mov_b32_e32 v176, v183
	v_mov_b32_e32 v183, v180
	v_pk_mul_f32 v[204:205], v[130:131], v[182:183] op_sel_hi:[0,1]
	s_waitcnt lgkmcnt(0)
	v_add_f32_e32 v129, v129, v172
	ds_bpermute_b32 v172, v185, v129
	v_mov_b32_e32 v180, 0
	v_cvt_pk_fp8_f32 v180, v204, v205
	v_mov_b32_e32 v177, v181
	v_pk_mul_f32 v[206:207], v[130:131], v[176:177] op_sel_hi:[0,1]
	s_waitcnt lgkmcnt(0)
	v_add_f32_e32 v129, v129, v172
	ds_bpermute_b32 v172, v186, v129
	v_cvt_pk_fp8_f32 v180, v206, v207 op_sel:[0,0,1]
	v_pk_mul_f32 v[176:177], v[130:131], v[170:171] op_sel_hi:[0,1]
	v_cvt_pk_fp8_f32 v174, v200, v201
	ds_write_b128 v195, v[176:179] offset:6144
	s_waitcnt lgkmcnt(1)
	v_add_f32_e32 v129, v129, v172
	ds_bpermute_b32 v172, v187, v129
	global_store_dword v[166:167], v180, off offset:-768
	v_cvt_pk_fp8_f32 v174, v202, v203 op_sel:[0,0,1]
	v_mov_b32_e32 v222, v221
	ds_write_b128 v195, v[200:203] offset:4096
	s_waitcnt lgkmcnt(1)
	v_add_f32_e32 v129, v129, v172
	ds_bpermute_b32 v172, v188, v129
	global_store_dword v[166:167], v174, off offset:-1024
	v_mov_b32_e32 v174, 0
	v_cvt_pk_fp8_f32 v174, v176, v177
	ds_write_b128 v195, v[204:207] offset:5120
	s_waitcnt lgkmcnt(1)
	v_add_f32_e32 v129, v129, v172
	ds_bpermute_b32 v180, v189, v129
	v_mov_b32_e32 v172, v175
	v_pk_mul_f32 v[170:171], v[172:173], v[130:131] op_sel_hi:[1,0]
	v_mov_b32_e32 v175, 0
	v_cvt_pk_fp8_f32 v175, v170, v171
	s_waitcnt lgkmcnt(0)
	v_add_f32_e32 v129, v129, v180
	v_fmamk_f32 v129, v129, 0x3a000000, v193
	v_cvt_pk_fp8_f32 v174, v178, v179 op_sel:[0,0,1]
	v_mov_b32_e32 v182, 0
	v_pk_mul_f32 v[172:173], v[168:169], v[130:131] op_sel_hi:[1,0]
	global_store_dword v[166:167], v174, off offset:-512
	v_cvt_pk_fp8_f32 v175, v172, v173 op_sel:[0,0,1]
	v_rsq_f32_e32 v130, v129
	global_store_dword v[166:167], v175, off offset:-256
	ds_write_b128 v195, v[170:173] offset:7168
	v_pk_mul_f32 v[174:175], v[130:131], v[208:209] op_sel_hi:[0,1]
	v_mov_b32_e32 v129, 0
	v_cvt_pk_fp8_f32 v129, v174, v175
	v_pk_mul_f32 v[176:177], v[130:131], v[210:211] op_sel_hi:[0,1]
	v_mov_b32_e32 v168, v213
	v_mov_b32_e32 v169, v215
	v_cvt_pk_fp8_f32 v129, v176, v177 op_sel:[0,0,1]
	v_pk_mul_f32 v[180:181], v[130:131], v[168:169] op_sel_hi:[0,1]
	ds_write_b128 v196, v[174:177]
	v_pk_mul_f32 v[168:169], v[130:131], v[216:217] op_sel_hi:[0,1]
	global_store_dword v[166:167], v129, off
	v_mov_b32_e32 v129, 0
	v_pk_mul_f32 v[172:173], v[222:223], v[130:131] op_sel_hi:[1,0]
	v_mov_b32_e32 v176, 0
	v_cvt_pk_fp8_f32 v129, v168, v169
	v_cvt_pk_fp8_f32 v176, v172, v173
	v_mov_b32_e32 v213, v214
	v_pk_mul_f32 v[178:179], v[130:131], v[212:213] op_sel_hi:[0,1]
	v_pk_mul_f32 v[170:171], v[130:131], v[218:219] op_sel_hi:[0,1]
	v_pk_mul_f32 v[174:175], v[224:225], v[130:131] op_sel_hi:[1,0]
	v_cvt_pk_fp8_f32 v182, v178, v179
	v_cvt_pk_fp8_f32 v129, v170, v171 op_sel:[0,0,1]
	v_cvt_pk_fp8_f32 v176, v174, v175 op_sel:[0,0,1]
	ds_write_b128 v196, v[178:181] offset:1024
	ds_write_b128 v196, v[168:171] offset:2048
	v_mov_b32_e32 v168, v227
	v_mov_b32_e32 v169, v229
	v_mov_b32_e32 v227, v228
	v_mov_b32_e32 v178, v231
	v_mov_b32_e32 v231, v232
	v_cvt_pk_fp8_f32 v182, v180, v181 op_sel:[0,0,1]
	global_store_dword v[166:167], v129, off offset:512
	global_store_dword v[166:167], v176, off offset:768
	v_pk_mul_f32 v[170:171], v[130:131], v[168:169] op_sel_hi:[0,1]
	v_pk_mul_f32 v[168:169], v[130:131], v[226:227] op_sel_hi:[0,1]
	v_mov_b32_e32 v129, 0
	v_pk_mul_f32 v[176:177], v[130:131], v[230:231] op_sel_hi:[0,1]
	v_mov_b32_e32 v180, 0
	v_cvt_pk_fp8_f32 v129, v168, v169
	v_cvt_pk_fp8_f32 v180, v176, v177
	v_mov_b32_e32 v179, v233
	v_pk_mul_f32 v[178:179], v[130:131], v[178:179] op_sel_hi:[0,1]
	v_cvt_pk_fp8_f32 v129, v170, v171 op_sel:[0,0,1]
	v_cvt_pk_fp8_f32 v180, v178, v179 op_sel:[0,0,1]
	ds_write_b128 v196, v[172:175] offset:3072
	ds_write_b128 v196, v[168:171] offset:4096
	global_store_dword v[166:167], v129, off offset:1024
	global_store_dword v[166:167], v180, off offset:1280
	v_pk_mul_f32 v[168:169], v[130:131], v[234:235] op_sel_hi:[0,1]
	v_mov_b32_e32 v129, 0
	v_pk_mul_f32 v[172:173], v[240:241], v[130:131] op_sel_hi:[1,0]
	v_mov_b32_e32 v180, 0
	v_cvt_pk_fp8_f32 v129, v168, v169
	v_cvt_pk_fp8_f32 v180, v172, v173
	v_pk_mul_f32 v[170:171], v[130:131], v[236:237] op_sel_hi:[0,1]
	v_pk_mul_f32 v[174:175], v[242:243], v[130:131] op_sel_hi:[1,0]
	v_cvt_pk_fp8_f32 v129, v170, v171 op_sel:[0,0,1]
	v_cvt_pk_fp8_f32 v180, v174, v175 op_sel:[0,0,1]
	s_and_b64 vcc, exec, s[34:35]
	global_store_dword v[166:167], v182, off offset:256
	ds_write_b128 v196, v[176:179] offset:5120
	global_store_dword v[166:167], v129, off offset:1536
	ds_write_b128 v196, v[168:171] offset:6144
	global_store_dword v[166:167], v180, off offset:1792
	ds_write_b128 v196, v[172:175] offset:7168
	s_waitcnt lgkmcnt(0)
	s_barrier
	s_cbranch_vccnz .LBB0_975
	s_ashr_i32 s31, s30, 31
	s_lshl_b64 s[12:13], s[30:31], 16
	v_mbcnt_lo_u32_b32 v129, -1, 0
	v_mbcnt_hi_u32_b32 v129, -1, v129
	s_add_u32 s12, s1, s12
	v_lshlrev_b32_e32 v129, 3, v129
	s_addc_u32 s13, s2, s13
	v_and_b32_e32 v130, 0x7ffffff8, v129
	v_lshl_add_u64 v[132:133], s[12:13], 0, v[130:131]
	v_add_co_u32_e32 v148, vcc, s41, v132
	v_lshl_add_u64 v[160:161], v[132:133], 0, s[28:29]
	s_nop 0
	v_addc_co_u32_e32 v149, vcc, 0, v133, vcc
	global_load_dwordx2 v[132:133], v130, s[12:13]
	global_load_dwordx2 v[134:135], v130, s[12:13] offset:512
	global_load_dwordx2 v[140:141], v130, s[12:13] offset:1024
	global_load_dwordx2 v[144:145], v130, s[12:13] offset:1536
	global_load_dwordx2 v[136:137], v[160:161], off offset:512
	global_load_dwordx2 v[138:139], v[160:161], off offset:1024
	global_load_dwordx2 v[142:143], v[160:161], off offset:1536
	global_load_dwordx2 v[146:147], v[160:161], off offset:2048
	global_load_dwordx2 v[150:151], v130, s[12:13] offset:2048
	global_load_dwordx2 v[152:153], v130, s[12:13] offset:2560
	global_load_dwordx2 v[156:157], v130, s[12:13] offset:3072
	global_load_dwordx2 v[162:163], v130, s[12:13] offset:3584
	s_nop 0
	global_load_dwordx2 v[148:149], v[148:149], off
	s_nop 0
	global_load_dwordx2 v[154:155], v[160:161], off offset:2560
	global_load_dwordx2 v[158:159], v[160:161], off offset:3072
	s_nop 0
	global_load_dwordx2 v[160:161], v[160:161], off offset:3584
